# on the combination: no producer items for the pre-converted groups (prefix tables + decode), converter items claim the next ticket before the image-store drain (no atomic round trip after the flag sto
# speedup vs baseline: 1.0135x; 1.0023x over previous
; #define LAS3 __attribute__((address_space(3)))
; __device__ __forceinline__ int lane_id() { int r; asm volatile("v_mbcnt_lo_u32_b32 %0, -1, 0\n\tv_mbcnt_hi_u32_b32 %0, -1, %0" : "=v"(r)); return r; }
; template <int EPI>
; __device__ __forceinline__ int* moe_phase(const Params& p, LAS3 char* lds, int wid, int* pend_in) {
;     ...
;     { const int t0 = wid * 64 + lane_id();
;       if (t0 < 8) { int a = 0; LAS3 int* pq = pre + t0 * 128;
;           for (int s = 0; s <= NSL; ++s) { pq[s] = a;
;               if (s < NSL) { int nv = (s < NS && mtv[t0 + 8 * (s / NCOL)] > 0) ? 1 : 0; const int sc = s - MOE_LAG;
;                   if (EPI == 2 && s < MOE_LAG3 && mtv[t0 + 8 * (s >> 3)] > 0) nv += 1;
;                   if (sc >= 0 && sc < NS) nv += mtv[t0 + 8 * (sc / NCOL)];
;                   a += nv; } } } }
.LBB0_410:
	s_or_b64 exec, exec, s[0:1]
	v_mbcnt_lo_u32_b32 v2, -1, 0
	v_mbcnt_hi_u32_b32 v2, -1, v2
	s_nop 0
	v_add_u32_e32 v0, s75, v2
	v_cmp_gt_i32_e32 vcc, 8, v0
	s_and_saveexec_b64 s[0:1], vcc
	s_cbranch_execz .LBB0_428
	s_waitcnt vmcnt(0)
	v_lshl_add_u32 v1, v0, 9, 0
	v_add_u32_e32 v1, 0x22000, v1
	v_lshl_add_u32 v3, v0, 2, 0
	v_add_u32_e32 v3, 0x21300, v3
	ds_read_b32 v4, v3
	ds_read_b32 v5, v3 offset:32
	ds_read_b32 v6, v3 offset:64
	ds_read_b32 v7, v3 offset:96
	v_mov_b32_e32 v2, 0
	s_waitcnt lgkmcnt(0)
	v_mov_b32_e32 v3, 0
	ds_write_b32 v1, v2
	v_add_u32_e32 v2, v2, v3
	ds_write_b32 v1, v2 offset:4
	v_add_u32_e32 v2, v2, v3
	ds_write_b32 v1, v2 offset:8
	v_add_u32_e32 v2, v2, v3
	ds_write_b32 v1, v2 offset:12
	v_add_u32_e32 v2, v2, v3
	ds_write_b32 v1, v2 offset:16
	v_add_u32_e32 v2, v2, v3
	ds_write_b32 v1, v2 offset:20
	v_add_u32_e32 v2, v2, v3
	ds_write_b32 v1, v2 offset:24
	v_add_u32_e32 v2, v2, v3
	ds_write_b32 v1, v2 offset:28
	v_add_u32_e32 v2, v2, v3
	ds_write_b32 v1, v2 offset:32
	v_add_u32_e32 v2, v2, v3
	ds_write_b32 v1, v2 offset:36
	v_add_u32_e32 v2, v2, v3
	ds_write_b32 v1, v2 offset:40
	v_add_u32_e32 v2, v2, v3
	ds_write_b32 v1, v2 offset:44
	v_add_u32_e32 v2, v2, v3
	ds_write_b32 v1, v2 offset:48
	v_add_u32_e32 v2, v2, v3
	ds_write_b32 v1, v2 offset:52
	v_add_u32_e32 v2, v2, v3
	ds_write_b32 v1, v2 offset:56
	v_add_u32_e32 v2, v2, v3
	v_mov_b32_e32 v3, v4
	ds_write_b32 v1, v2 offset:60
	v_add_u32_e32 v2, v2, v3
	v_cmp_lt_i32_e32 vcc, 0, v5
	s_nop 1
	v_addc_co_u32_e32 v3, vcc, 0, v4, vcc
	ds_write_b32 v1, v2 offset:64
	v_add_u32_e32 v2, v2, v3
	ds_write_b32 v1, v2 offset:68
	v_add_u32_e32 v2, v2, v3
	ds_write_b32 v1, v2 offset:72
	v_add_u32_e32 v2, v2, v3
	ds_write_b32 v1, v2 offset:76
	v_add_u32_e32 v2, v2, v3
	ds_write_b32 v1, v2 offset:80
	v_add_u32_e32 v2, v2, v3
	ds_write_b32 v1, v2 offset:84
	v_add_u32_e32 v2, v2, v3
	ds_write_b32 v1, v2 offset:88
	v_add_u32_e32 v2, v2, v3
	ds_write_b32 v1, v2 offset:92
	v_add_u32_e32 v2, v2, v3
	ds_write_b32 v1, v2 offset:96
	v_add_u32_e32 v2, v2, v3
	ds_write_b32 v1, v2 offset:100
	v_add_u32_e32 v2, v2, v3
	ds_write_b32 v1, v2 offset:104
	v_add_u32_e32 v2, v2, v3
	ds_write_b32 v1, v2 offset:108
	v_add_u32_e32 v2, v2, v3
	ds_write_b32 v1, v2 offset:112
	v_add_u32_e32 v2, v2, v3
	ds_write_b32 v1, v2 offset:116
	v_add_u32_e32 v2, v2, v3
	ds_write_b32 v1, v2 offset:120
	v_add_u32_e32 v2, v2, v3
	v_cmp_lt_i32_e32 vcc, 0, v5
	s_nop 1
	v_addc_co_u32_e32 v3, vcc, 0, v5, vcc
	ds_write_b32 v1, v2 offset:124
	v_add_u32_e32 v2, v2, v3
	v_cmp_lt_i32_e32 vcc, 0, v6
	s_nop 1
	v_addc_co_u32_e32 v3, vcc, 0, v5, vcc
	ds_write_b32 v1, v2 offset:128
	v_add_u32_e32 v2, v2, v3
	ds_write_b32 v1, v2 offset:132
	v_add_u32_e32 v2, v2, v3
	ds_write_b32 v1, v2 offset:136
	v_add_u32_e32 v2, v2, v3
	ds_write_b32 v1, v2 offset:140
	v_add_u32_e32 v2, v2, v3
	ds_write_b32 v1, v2 offset:144
	v_add_u32_e32 v2, v2, v3
	ds_write_b32 v1, v2 offset:148
	v_add_u32_e32 v2, v2, v3
	ds_write_b32 v1, v2 offset:152
	v_add_u32_e32 v2, v2, v3
	ds_write_b32 v1, v2 offset:156
	v_add_u32_e32 v2, v2, v3
	ds_write_b32 v1, v2 offset:160
	v_add_u32_e32 v2, v2, v3
	ds_write_b32 v1, v2 offset:164
	v_add_u32_e32 v2, v2, v3
	ds_write_b32 v1, v2 offset:168
	v_add_u32_e32 v2, v2, v3
	ds_write_b32 v1, v2 offset:172
	v_add_u32_e32 v2, v2, v3
	ds_write_b32 v1, v2 offset:176
	v_add_u32_e32 v2, v2, v3
	ds_write_b32 v1, v2 offset:180
	v_add_u32_e32 v2, v2, v3
	ds_write_b32 v1, v2 offset:184
	v_add_u32_e32 v2, v2, v3
	v_cmp_lt_i32_e32 vcc, 0, v6
	s_nop 1
	v_addc_co_u32_e32 v3, vcc, 0, v6, vcc
	ds_write_b32 v1, v2 offset:188
	v_add_u32_e32 v2, v2, v3
	v_cmp_lt_i32_e32 vcc, 0, v7
	s_nop 1
	v_addc_co_u32_e32 v3, vcc, 0, v6, vcc
	ds_write_b32 v1, v2 offset:192
	v_add_u32_e32 v2, v2, v3
	ds_write_b32 v1, v2 offset:196
	v_add_u32_e32 v2, v2, v3
	ds_write_b32 v1, v2 offset:200
	v_add_u32_e32 v2, v2, v3
	ds_write_b32 v1, v2 offset:204
	v_add_u32_e32 v2, v2, v3
	ds_write_b32 v1, v2 offset:208
	v_add_u32_e32 v2, v2, v3
	ds_write_b32 v1, v2 offset:212
	v_add_u32_e32 v2, v2, v3
	ds_write_b32 v1, v2 offset:216
	v_add_u32_e32 v2, v2, v3
	ds_write_b32 v1, v2 offset:220
	v_add_u32_e32 v2, v2, v3
	ds_write_b32 v1, v2 offset:224
	v_add_u32_e32 v2, v2, v3
	ds_write_b32 v1, v2 offset:228
	v_add_u32_e32 v2, v2, v3
	ds_write_b32 v1, v2 offset:232
	v_add_u32_e32 v2, v2, v3
	ds_write_b32 v1, v2 offset:236
	v_add_u32_e32 v2, v2, v3
	ds_write_b32 v1, v2 offset:240
	v_add_u32_e32 v2, v2, v3
	ds_write_b32 v1, v2 offset:244
	v_add_u32_e32 v2, v2, v3
	ds_write_b32 v1, v2 offset:248
	v_add_u32_e32 v2, v2, v3
	v_cmp_lt_i32_e32 vcc, 0, v7
	s_nop 1
	v_addc_co_u32_e32 v3, vcc, 0, v7, vcc
	ds_write_b32 v1, v2 offset:252
	v_add_u32_e32 v2, v2, v3
	v_mov_b32_e32 v3, v7
	ds_write_b32 v1, v2 offset:256
	v_add_u32_e32 v2, v2, v3
	ds_write_b32 v1, v2 offset:260
	v_add_u32_e32 v2, v2, v3
	ds_write_b32 v1, v2 offset:264
	v_add_u32_e32 v2, v2, v3
	ds_write_b32 v1, v2 offset:268
	v_add_u32_e32 v2, v2, v3
	ds_write_b32 v1, v2 offset:272
	v_add_u32_e32 v2, v2, v3
	ds_write_b32 v1, v2 offset:276
	v_add_u32_e32 v2, v2, v3
	ds_write_b32 v1, v2 offset:280
	v_add_u32_e32 v2, v2, v3
	ds_write_b32 v1, v2 offset:284
	v_add_u32_e32 v2, v2, v3
	ds_write_b32 v1, v2 offset:288
	v_add_u32_e32 v2, v2, v3
	ds_write_b32 v1, v2 offset:292
	v_add_u32_e32 v2, v2, v3
	ds_write_b32 v1, v2 offset:296
	v_add_u32_e32 v2, v2, v3
	ds_write_b32 v1, v2 offset:300
	v_add_u32_e32 v2, v2, v3
	ds_write_b32 v1, v2 offset:304
	v_add_u32_e32 v2, v2, v3
	ds_write_b32 v1, v2 offset:308
	v_add_u32_e32 v2, v2, v3
	ds_write_b32 v1, v2 offset:312
	v_add_u32_e32 v2, v2, v3
	ds_write_b32 v1, v2 offset:316

; __device__ __forceinline__ int lane_id() { int r; asm volatile("v_mbcnt_lo_u32_b32 %0, -1, 0\n\tv_mbcnt_hi_u32_b32 %0, -1, %0" : "=v"(r)); return r; }
; template <int EPI>
; __device__ __forceinline__ int* moe_phase(const Params& p, LAS3 char* lds, int wid, int* pend_in) {
;     ...
;             { const int l = lane_id();
;               const bool c1 = (l + 1 <= NSL) && (pq[(l + 1 <= NSL) ? l + 1 : 0] <= i), c2 = (l + 65 <= NSL) && (pq[(l + 65 <= NSL) ? l + 65 : 0] <= i);
;               s = __builtin_popcountll(__builtin_amdgcn_ballot_w64(c1)) + __builtin_popcountll(__builtin_amdgcn_ballot_w64(c2));
;               j = i - __builtin_amdgcn_readfirstlane(pq[s]); }
;             const bool hasP = (s < NS) && (__builtin_amdgcn_readfirstlane(mtv[qq + 8 * ((s < NS) ? s / NCOL : 0)]) > 0);
.LBB0_446:
	s_or_b64 exec, exec, s[16:17]
	v_cndmask_b32_e64 v0, 0, 1, s[14:15]
	v_cmp_ne_u32_e32 vcc, 0, v0
	v_cndmask_b32_e64 v0, 0, 1, s[0:1]
	s_bcnt1_i32_b64 s4, vcc
	v_cmp_ne_u32_e32 vcc, 0, v0
	s_bcnt1_i32_b64 s12, vcc
	s_add_i32 s12, s12, s4
	s_lshl_b32 s0, s12, 2
	s_add_i32 s0, s24, s0
	v_mov_b32_e32 v0, s0
	ds_read_b32 v0, v0
	s_mov_b64 s[0:1], 0
	s_cmp_gt_u32 s12, 63
	s_mov_b64 s[24:25], 0
	s_waitcnt lgkmcnt(0)
	v_readfirstlane_b32 s4, v0
	s_cbranch_scc1 .LBB0_448
	s_cmp_lt_u32 s12, 16
	s_cbranch_scc1 .LBB0_448
	s_lshl_b32 s13, s86, 2
	s_lshl_b32 s14, s12, 1
	s_add_i32 s13, s13, 0
	s_and_b32 s14, s14, 0x60
	s_add_i32 s13, s13, s14
	s_add_i32 s13, s13, 0x21300
	v_mov_b32_e32 v0, s13
	ds_read_b32 v0, v0
	s_waitcnt lgkmcnt(0)
	v_readfirstlane_b32 s13, v0
	s_cmp_gt_i32 s13, 0
	s_cselect_b64 s[24:25], -1, 0

; __device__ __forceinline__ int lane_id() { int r; asm volatile("v_mbcnt_lo_u32_b32 %0, -1, 0\n\tv_mbcnt_hi_u32_b32 %0, -1, %0" : "=v"(r)); return r; }
; #define LD_WAIT(r) asm volatile("s_waitcnt vmcnt(0)" : "+v"(r) :: "memory")
; __device__ __forceinline__ int ld_now(const int* ptr) { int r = ld_early(ptr); LD_WAIT(r); return r; }
; template <int LDB>
; __device__ __forceinline__ void convert_image(const float* __restrict__ W, int col0, int col1, unsigned char* __restrict__ img, LAS3 char* lds, int wid) {
;     ...
;     asm volatile("s_waitcnt vmcnt(0)" ::: "memory");
;     __syncthreads();
; template <int EPI>
; __device__ __forceinline__ int* moe_phase(const Params& p, LAS3 char* lds, int wid, int* pend_in) {
;     ...
;                         const bool have = (EPI == 3) && (__builtin_amdgcn_readfirstlane(ld_now(sy.flag)) != 0);
;                         if (have) { }
;                         else if (EPI == 2) convert_image<2 * DFF>(p.w_gate_up + (size_t)e * D * (2 * DFF), pn * 128, DFF + pn * 128, img, lds, wid);
;                         else convert_image<D>(p.w_down + (size_t)e * DFF * D, pn * 256, pn * 256 + 128, img, lds, wid);
;                         const int t0 = wid * 64 + lane_id();
;                         if (t0 == 0) { __hip_atomic_store(sy.flag, 1, __ATOMIC_RELAXED, __HIP_MEMORY_SCOPE_AGENT); unsigned c0 = inc_early(&qctr[qq]); LD_WAIT(c0); slot[par ^ 1] = ((unsigned)qq << 20) | c0; }
.Lgu_have:
	v_mbcnt_lo_u32_b32 v148, -1, 0
	v_mbcnt_hi_u32_b32 v148, -1, v148
	s_nop 0
	v_sub_u32_e32 v148, 0, v148
	v_cmp_eq_u32_e32 vcc, s75, v148
	s_and_saveexec_b64 s[0:1], vcc
	s_cbranch_execz .Ltkc_gu
	v_readlane_b32 s100, v255, 17
	v_readlane_b32 s101, v255, 18
	v_mov_b32_e32 v148, 0
	v_mov_b32_e32 v151, 1
	s_nop 4
	global_atomic_add v151, v148, v151, s[100:101] sc0
.Ltkc_gu:
	s_or_b64 exec, exec, s[0:1]
	s_waitcnt vmcnt(0)
	s_barrier
	s_waitcnt vmcnt(15)
	v_mbcnt_lo_u32_b32 v0, -1, 0
	v_mbcnt_hi_u32_b32 v0, -1, v0
	s_nop 0
	v_sub_u32_e32 v0, 0, v0
	v_cmp_eq_u32_e32 vcc, s75, v0
	s_and_saveexec_b64 s[0:1], vcc
	s_cbranch_execz .LBB0_493
	global_store_dword v150, v145, s[16:17] sc1
	v_readlane_b32 s4, v255, 19
	s_nop 1
	v_or_b32_e32 v0, s4, v151
	v_readlane_b32 s4, v255, 21
	s_nop 1
	v_mov_b32_e32 v1, s4
	ds_write_b32 v1, v0

; #define LAS3 __attribute__((address_space(3)))
; __device__ __forceinline__ int lane_id() { int r; asm volatile("v_mbcnt_lo_u32_b32 %0, -1, 0\n\tv_mbcnt_hi_u32_b32 %0, -1, %0" : "=v"(r)); return r; }
; template <int EPI>
; __device__ __forceinline__ int* moe_phase(const Params& p, LAS3 char* lds, int wid, int* pend_in) {
;     ...
;     { const int t0 = wid * 64 + lane_id();
;       if (t0 < 8) { int a = 0; LAS3 int* pq = pre + t0 * 128;
;           for (int s = 0; s <= NSL; ++s) { pq[s] = a;
;               if (s < NSL) { int nv = (s < NS && mtv[t0 + 8 * (s / NCOL)] > 0) ? 1 : 0; const int sc = s - MOE_LAG;
;                   if (EPI == 2 && s < MOE_LAG3 && mtv[t0 + 8 * (s >> 3)] > 0) nv += 1;
;                   if (sc >= 0 && sc < NS) nv += mtv[t0 + 8 * (sc / NCOL)];
;                   a += nv; } } } }
.LBB0_514:
	s_or_b64 exec, exec, s[0:1]
	v_mbcnt_lo_u32_b32 v0, -1, 0
	v_mbcnt_hi_u32_b32 v0, -1, v0
	s_nop 0
	v_add_u32_e32 v0, s75, v0
	v_cmp_gt_i32_e32 vcc, 8, v0
	s_and_saveexec_b64 s[0:1], vcc
	s_cbranch_execz .LBB0_516
	s_waitcnt vmcnt(0)
	v_lshl_add_u32 v1, v0, 9, 0
	v_add_u32_e32 v1, 0x22000, v1
	v_lshl_add_u32 v3, v0, 2, 0
	v_add_u32_e32 v3, 0x21300, v3
	ds_read_b32 v4, v3
	ds_read_b32 v5, v3 offset:32
	ds_read_b32 v6, v3 offset:64
	ds_read_b32 v7, v3 offset:96
	v_mov_b32_e32 v2, 0
	s_waitcnt lgkmcnt(0)
	v_mov_b32_e32 v3, 0
	ds_write_b32 v1, v2
	v_add_u32_e32 v2, v2, v3
	ds_write_b32 v1, v2 offset:4
	v_add_u32_e32 v2, v2, v3
	ds_write_b32 v1, v2 offset:8
	v_add_u32_e32 v2, v2, v3
	ds_write_b32 v1, v2 offset:12
	v_add_u32_e32 v2, v2, v3
	ds_write_b32 v1, v2 offset:16
	v_add_u32_e32 v2, v2, v3
	ds_write_b32 v1, v2 offset:20
	v_add_u32_e32 v2, v2, v3
	ds_write_b32 v1, v2 offset:24
	v_add_u32_e32 v2, v2, v3
	ds_write_b32 v1, v2 offset:28
	v_add_u32_e32 v2, v2, v3
	ds_write_b32 v1, v2 offset:32
	v_add_u32_e32 v2, v2, v3
	ds_write_b32 v1, v2 offset:36
	v_add_u32_e32 v2, v2, v3
	ds_write_b32 v1, v2 offset:40
	v_add_u32_e32 v2, v2, v3
	ds_write_b32 v1, v2 offset:44
	v_add_u32_e32 v2, v2, v3
	ds_write_b32 v1, v2 offset:48
	v_add_u32_e32 v2, v2, v3
	ds_write_b32 v1, v2 offset:52
	v_add_u32_e32 v2, v2, v3
	ds_write_b32 v1, v2 offset:56
	v_add_u32_e32 v2, v2, v3
	v_mov_b32_e32 v3, v4
	ds_write_b32 v1, v2 offset:60
	v_add_u32_e32 v2, v2, v3
	v_cmp_lt_i32_e32 vcc, 0, v6
	s_nop 1
	v_addc_co_u32_e32 v3, vcc, 0, v4, vcc
	ds_write_b32 v1, v2 offset:64
	v_add_u32_e32 v2, v2, v3
	ds_write_b32 v1, v2 offset:68
	v_add_u32_e32 v2, v2, v3
	ds_write_b32 v1, v2 offset:72
	v_add_u32_e32 v2, v2, v3
	ds_write_b32 v1, v2 offset:76
	v_add_u32_e32 v2, v2, v3
	ds_write_b32 v1, v2 offset:80
	v_add_u32_e32 v2, v2, v3
	ds_write_b32 v1, v2 offset:84
	v_add_u32_e32 v2, v2, v3
	ds_write_b32 v1, v2 offset:88
	v_add_u32_e32 v2, v2, v3
	v_cmp_lt_i32_e32 vcc, 0, v6
	s_nop 1
	v_addc_co_u32_e32 v3, vcc, 0, v5, vcc
	ds_write_b32 v1, v2 offset:92
	v_add_u32_e32 v2, v2, v3
	v_cmp_lt_i32_e32 vcc, 0, v7
	s_nop 1
	v_addc_co_u32_e32 v3, vcc, 0, v5, vcc
	ds_write_b32 v1, v2 offset:96
	v_add_u32_e32 v2, v2, v3
	ds_write_b32 v1, v2 offset:100
	v_add_u32_e32 v2, v2, v3
	ds_write_b32 v1, v2 offset:104
	v_add_u32_e32 v2, v2, v3
	ds_write_b32 v1, v2 offset:108
	v_add_u32_e32 v2, v2, v3
	ds_write_b32 v1, v2 offset:112
	v_add_u32_e32 v2, v2, v3
	ds_write_b32 v1, v2 offset:116
	v_add_u32_e32 v2, v2, v3
	ds_write_b32 v1, v2 offset:120
	v_add_u32_e32 v2, v2, v3
	v_cmp_lt_i32_e32 vcc, 0, v7
	s_nop 1
	v_addc_co_u32_e32 v3, vcc, 0, v6, vcc
	ds_write_b32 v1, v2 offset:124
	v_add_u32_e32 v2, v2, v3
	v_mov_b32_e32 v3, v6
	ds_write_b32 v1, v2 offset:128
	v_add_u32_e32 v2, v2, v3
	ds_write_b32 v1, v2 offset:132
	v_add_u32_e32 v2, v2, v3
	ds_write_b32 v1, v2 offset:136
	v_add_u32_e32 v2, v2, v3
	ds_write_b32 v1, v2 offset:140
	v_add_u32_e32 v2, v2, v3
	ds_write_b32 v1, v2 offset:144
	v_add_u32_e32 v2, v2, v3
	ds_write_b32 v1, v2 offset:148
	v_add_u32_e32 v2, v2, v3
	ds_write_b32 v1, v2 offset:152
	v_add_u32_e32 v2, v2, v3
	v_mov_b32_e32 v3, v7
	ds_write_b32 v1, v2 offset:156
	v_add_u32_e32 v2, v2, v3
	ds_write_b32 v1, v2 offset:160
	v_add_u32_e32 v2, v2, v3
	ds_write_b32 v1, v2 offset:164
	v_add_u32_e32 v2, v2, v3
	ds_write_b32 v1, v2 offset:168
	v_add_u32_e32 v2, v2, v3
	ds_write_b32 v1, v2 offset:172
	v_add_u32_e32 v2, v2, v3
	ds_write_b32 v1, v2 offset:176
	v_add_u32_e32 v2, v2, v3
	ds_write_b32 v1, v2 offset:180
	v_add_u32_e32 v2, v2, v3
	ds_write_b32 v1, v2 offset:184
	v_add_u32_e32 v2, v2, v3
	ds_write_b32 v1, v2 offset:188

; __device__ __forceinline__ int lane_id() { int r; asm volatile("v_mbcnt_lo_u32_b32 %0, -1, 0\n\tv_mbcnt_hi_u32_b32 %0, -1, %0" : "=v"(r)); return r; }
; template <int EPI>
; __device__ __forceinline__ int* moe_phase(const Params& p, LAS3 char* lds, int wid, int* pend_in) {
;     ...
;             { const int l = lane_id();
;               const bool c1 = (l + 1 <= NSL) && (pq[(l + 1 <= NSL) ? l + 1 : 0] <= i), c2 = (l + 65 <= NSL) && (pq[(l + 65 <= NSL) ? l + 65 : 0] <= i);
;               s = __builtin_popcountll(__builtin_amdgcn_ballot_w64(c1)) + __builtin_popcountll(__builtin_amdgcn_ballot_w64(c2));
;               j = i - __builtin_amdgcn_readfirstlane(pq[s]); }
;             const bool hasP = (s < NS) && (__builtin_amdgcn_readfirstlane(mtv[qq + 8 * ((s < NS) ? s / NCOL : 0)]) > 0);
.LBB0_534:
	s_or_b64 exec, exec, s[28:29]
	v_cndmask_b32_e64 v0, 0, 1, s[26:27]
	v_cmp_ne_u32_e32 vcc, 0, v0
	v_cndmask_b32_e64 v0, 0, 1, s[0:1]
	s_bcnt1_i32_b64 s4, vcc
	v_cmp_ne_u32_e32 vcc, 0, v0
	s_bcnt1_i32_b64 s0, vcc
	s_add_i32 s4, s0, s4
	s_lshl_b32 s0, s4, 2
	s_add_i32 s0, s14, s0
	v_mov_b32_e32 v0, s0
	ds_read_b32 v0, v0
	s_mov_b64 s[26:27], 0
	s_cmp_gt_u32 s4, 31
	s_mov_b64 s[30:31], 0
	s_waitcnt lgkmcnt(0)
	v_readfirstlane_b32 s34, v0
	s_cbranch_scc1 .LBB0_536
	s_cmp_lt_u32 s4, 16
	s_cbranch_scc1 .LBB0_536
	s_lshl_b32 s0, s19, 2
	s_and_b32 s1, s4, 24
	s_add_i32 s0, s0, 0
	s_lshl_b32 s1, s1, 2
	s_add_i32 s0, s0, s1
	s_add_i32 s0, s0, 0x21300
	v_mov_b32_e32 v0, s0
	ds_read_b32 v0, v0
	s_waitcnt lgkmcnt(0)
	v_readfirstlane_b32 s0, v0
	s_cmp_gt_i32 s0, 0
	s_cselect_b64 s[30:31], -1, 0

; __device__ __forceinline__ int lane_id() { int r; asm volatile("v_mbcnt_lo_u32_b32 %0, -1, 0\n\tv_mbcnt_hi_u32_b32 %0, -1, %0" : "=v"(r)); return r; }
; #define LD_WAIT(r) asm volatile("s_waitcnt vmcnt(0)" : "+v"(r) :: "memory")
; template <int LDB>
; __device__ __forceinline__ void convert_image(const float* __restrict__ W, int col0, int col1, unsigned char* __restrict__ img, LAS3 char* lds, int wid) {
;     ...
;     asm volatile("s_waitcnt vmcnt(0)" ::: "memory");
;     __syncthreads();
; template <int EPI>
; __device__ __forceinline__ int* moe_phase(const Params& p, LAS3 char* lds, int wid, int* pend_in) {
;     ...
;                         else convert_image<D>(p.w_down + (size_t)e * DFF * D, pn * 256, pn * 256 + 128, img, lds, wid);
;                         const int t0 = wid * 64 + lane_id();
;                         if (t0 == 0) { __hip_atomic_store(sy.flag, 1, __ATOMIC_RELAXED, __HIP_MEMORY_SCOPE_AGENT); unsigned c0 = inc_early(&qctr[qq]); LD_WAIT(c0); slot[par ^ 1] = ((unsigned)qq << 20) | c0; }
.Ldn_have:
	v_mbcnt_lo_u32_b32 v153, -1, 0
	v_mbcnt_hi_u32_b32 v153, -1, v153
	s_nop 0
	v_sub_u32_e32 v153, 0, v153
	v_cmp_eq_u32_e32 vcc, s75, v153
	s_and_saveexec_b64 s[0:1], vcc
	s_cbranch_execz .Ltkc_dn
	v_mov_b32_e32 v153, 0
	v_mov_b32_e32 v154, 1
	s_nop 4
	global_atomic_add v154, v153, v154, s[28:29] sc0
.Ltkc_dn:
	s_or_b64 exec, exec, s[0:1]
	s_waitcnt vmcnt(0)
	s_barrier
.LBB0_591:
	s_waitcnt vmcnt(15)
	v_mbcnt_lo_u32_b32 v0, -1, 0
	v_mbcnt_hi_u32_b32 v0, -1, v0
	s_nop 0
	v_sub_u32_e32 v0, 0, v0
	v_cmp_eq_u32_e32 vcc, s75, v0
	s_and_saveexec_b64 s[0:1], vcc
	s_cbranch_execz .LBB0_519
	global_store_dword v145, v146, s[26:27] sc1
	s_nop 0
	s_nop 0
	v_or_b32_e32 v0, s11, v154
	v_mov_b32_e32 v1, s35
	ds_write_b32 v1, v0
	s_branch .LBB0_519
